# speedup vs baseline: 1.0065x; 1.0065x over previous
.LBB2_7:
	s_cmp_lt_u32 s94, 0x800
	s_cbranch_scc1 .Lg2_qk_epi
	s_branch .Lg2_v_epi

.Lg2_qk_epi:
	s_lshr_b32 s95, s50, 12
	s_lshl_b32 s95, s95, 9
	s_lshr_b32 s96, s94, 2
	s_add_u32 s95, s95, s96
	s_lshl_b32 s95, s95, 14
	s_add_u32 s96, s18, s95
	s_addc_u32 s97, s19, 0
	v_lshrrev_b32_e32 v200, 8, v0
	v_bfe_u32 v201, v0, 4, 2
	v_lshlrev_b32_e32 v200, 5, v200
	v_lshl_add_u32 v200, v201, 1, v200
	v_lshlrev_b32_e32 v200, 14, v200
	v_and_b32_e32 v202, 15, v0
	v_lshrrev_b32_e32 v201, 1, v0
	v_and_b32_e32 v201, 0x60, v201
	v_or3_b32 v202, v201, v202, s50
	v_and_b32_e32 v202, 0xfff, v202
	v_lshl_add_u32 v203, v202, 2, v200
	v_mov_b32_e32 v204, v203
	v_add_u32_e32 v205, 0x4000, v203
	v_add_u32_e32 v206, 0x20000, v203
	v_add_u32_e32 v207, 0x24000, v203
	v_add_u32_e32 v208, 0x40000, v203
	v_add_u32_e32 v209, 0x44000, v203
	v_add_u32_e32 v210, 0x60000, v203
	v_add_u32_e32 v211, 0x64000, v203
	v_fmamk_f32 v126, v126, 0x3a800000, v158
	v_fmamk_f32 v127, v127, 0x3a800000, v159
	v_fmamk_f32 v128, v128, 0x3a800000, v160
	v_fmamk_f32 v129, v129, 0x3a800000, v161
	v_fmamk_f32 v62, v62, 0x3a800000, v142
	v_fmamk_f32 v63, v63, 0x3a800000, v143
	v_fmamk_f32 v64, v64, 0x3a800000, v144
	v_fmamk_f32 v65, v65, 0x3a800000, v145
	v_cvt_pk_fp8_f32 v212, v126, v127
	v_cvt_pk_fp8_f32 v213, v128, v129
	v_cvt_pk_fp8_f32 v212, v62, v63 op_sel:[0,0,1]
	v_cvt_pk_fp8_f32 v213, v64, v65 op_sel:[0,0,1]
	v_fmamk_f32 v122, v122, 0x3a800000, v158
	v_fmamk_f32 v123, v123, 0x3a800000, v159
	v_fmamk_f32 v124, v124, 0x3a800000, v160
	v_fmamk_f32 v125, v125, 0x3a800000, v161
	v_fmamk_f32 v54, v54, 0x3a800000, v142
	v_fmamk_f32 v55, v55, 0x3a800000, v143
	v_fmamk_f32 v56, v56, 0x3a800000, v144
	v_fmamk_f32 v57, v57, 0x3a800000, v145
	global_store_dword v204, v212, s[96:97]
	global_store_dword v205, v213, s[96:97]
	v_cvt_pk_fp8_f32 v214, v122, v123
	v_cvt_pk_fp8_f32 v215, v124, v125
	v_cvt_pk_fp8_f32 v214, v54, v55 op_sel:[0,0,1]
	v_cvt_pk_fp8_f32 v215, v56, v57 op_sel:[0,0,1]
	v_fmamk_f32 v118, v118, 0x3a800000, v158
	v_fmamk_f32 v119, v119, 0x3a800000, v159
	v_fmamk_f32 v120, v120, 0x3a800000, v160
	v_fmamk_f32 v121, v121, 0x3a800000, v161
	v_fmamk_f32 v70, v70, 0x3a800000, v142
	v_fmamk_f32 v71, v71, 0x3a800000, v143
	v_fmamk_f32 v72, v72, 0x3a800000, v144
	v_fmamk_f32 v73, v73, 0x3a800000, v145
	global_store_dword v204, v214, s[96:97] offset:64
	global_store_dword v205, v215, s[96:97] offset:64
	v_cvt_pk_fp8_f32 v216, v118, v119
	v_cvt_pk_fp8_f32 v217, v120, v121
	v_cvt_pk_fp8_f32 v216, v70, v71 op_sel:[0,0,1]
	v_cvt_pk_fp8_f32 v217, v72, v73 op_sel:[0,0,1]
	v_fmamk_f32 v114, v114, 0x3a800000, v158
	v_fmamk_f32 v115, v115, 0x3a800000, v159
	v_fmamk_f32 v116, v116, 0x3a800000, v160
	v_fmamk_f32 v117, v117, 0x3a800000, v161
	v_fmamk_f32 v58, v58, 0x3a800000, v142
	v_fmamk_f32 v59, v59, 0x3a800000, v143
	v_fmamk_f32 v60, v60, 0x3a800000, v144
	v_fmamk_f32 v61, v61, 0x3a800000, v145
	global_store_dword v204, v216, s[96:97] offset:512
	global_store_dword v205, v217, s[96:97] offset:512
	v_cvt_pk_fp8_f32 v218, v114, v115
	v_cvt_pk_fp8_f32 v219, v116, v117
	v_cvt_pk_fp8_f32 v218, v58, v59 op_sel:[0,0,1]
	v_cvt_pk_fp8_f32 v219, v60, v61 op_sel:[0,0,1]
	v_fmamk_f32 v110, v110, 0x3a800000, v154
	v_fmamk_f32 v111, v111, 0x3a800000, v155
	v_fmamk_f32 v112, v112, 0x3a800000, v156
	v_fmamk_f32 v113, v113, 0x3a800000, v157
	v_fmamk_f32 v42, v42, 0x3a800000, v138
	v_fmamk_f32 v43, v43, 0x3a800000, v139
	v_fmamk_f32 v44, v44, 0x3a800000, v140
	v_fmamk_f32 v45, v45, 0x3a800000, v141
	global_store_dword v204, v218, s[96:97] offset:576
	global_store_dword v205, v219, s[96:97] offset:576
	v_cvt_pk_fp8_f32 v220, v110, v111
	v_cvt_pk_fp8_f32 v221, v112, v113
	v_cvt_pk_fp8_f32 v220, v42, v43 op_sel:[0,0,1]
	v_cvt_pk_fp8_f32 v221, v44, v45 op_sel:[0,0,1]
	v_fmamk_f32 v98, v98, 0x3a800000, v154
	v_fmamk_f32 v99, v99, 0x3a800000, v155
	v_fmamk_f32 v100, v100, 0x3a800000, v156
	v_fmamk_f32 v101, v101, 0x3a800000, v157
	v_fmamk_f32 v34, v34, 0x3a800000, v138
	v_fmamk_f32 v35, v35, 0x3a800000, v139
	v_fmamk_f32 v36, v36, 0x3a800000, v140
	v_fmamk_f32 v37, v37, 0x3a800000, v141
	global_store_dword v206, v220, s[96:97]
	global_store_dword v207, v221, s[96:97]
	v_cvt_pk_fp8_f32 v222, v98, v99
	v_cvt_pk_fp8_f32 v223, v100, v101
	v_cvt_pk_fp8_f32 v222, v34, v35 op_sel:[0,0,1]
	v_cvt_pk_fp8_f32 v223, v36, v37 op_sel:[0,0,1]
	v_fmamk_f32 v106, v106, 0x3a800000, v154
	v_fmamk_f32 v107, v107, 0x3a800000, v155
	v_fmamk_f32 v108, v108, 0x3a800000, v156
	v_fmamk_f32 v109, v109, 0x3a800000, v157
	v_fmamk_f32 v46, v46, 0x3a800000, v138
	v_fmamk_f32 v47, v47, 0x3a800000, v139
	v_fmamk_f32 v48, v48, 0x3a800000, v140
	v_fmamk_f32 v49, v49, 0x3a800000, v141
	global_store_dword v206, v222, s[96:97] offset:64
	global_store_dword v207, v223, s[96:97] offset:64
	v_cvt_pk_fp8_f32 v224, v106, v107
	v_cvt_pk_fp8_f32 v225, v108, v109
	v_cvt_pk_fp8_f32 v224, v46, v47 op_sel:[0,0,1]
	v_cvt_pk_fp8_f32 v225, v48, v49 op_sel:[0,0,1]
	v_fmamk_f32 v102, v102, 0x3a800000, v154
	v_fmamk_f32 v103, v103, 0x3a800000, v155
	v_fmamk_f32 v104, v104, 0x3a800000, v156
	v_fmamk_f32 v105, v105, 0x3a800000, v157
	v_fmamk_f32 v38, v38, 0x3a800000, v138
	v_fmamk_f32 v39, v39, 0x3a800000, v139
	v_fmamk_f32 v40, v40, 0x3a800000, v140
	v_fmamk_f32 v41, v41, 0x3a800000, v141
	global_store_dword v206, v224, s[96:97] offset:512
	global_store_dword v207, v225, s[96:97] offset:512
	v_cvt_pk_fp8_f32 v226, v102, v103
	v_cvt_pk_fp8_f32 v227, v104, v105
	v_cvt_pk_fp8_f32 v226, v38, v39 op_sel:[0,0,1]
	v_cvt_pk_fp8_f32 v227, v40, v41 op_sel:[0,0,1]
	v_fmamk_f32 v86, v86, 0x3a800000, v150
	v_fmamk_f32 v87, v87, 0x3a800000, v151
	v_fmamk_f32 v88, v88, 0x3a800000, v152
	v_fmamk_f32 v89, v89, 0x3a800000, v153
	v_fmamk_f32 v26, v26, 0x3a800000, v134
	v_fmamk_f32 v27, v27, 0x3a800000, v135
	v_fmamk_f32 v28, v28, 0x3a800000, v136
	v_fmamk_f32 v29, v29, 0x3a800000, v137
	global_store_dword v206, v226, s[96:97] offset:576
	global_store_dword v207, v227, s[96:97] offset:576
	v_cvt_pk_fp8_f32 v228, v86, v87
	v_cvt_pk_fp8_f32 v229, v88, v89
	v_cvt_pk_fp8_f32 v228, v26, v27 op_sel:[0,0,1]
	v_cvt_pk_fp8_f32 v229, v28, v29 op_sel:[0,0,1]
	v_fmamk_f32 v82, v82, 0x3a800000, v150
	v_fmamk_f32 v83, v83, 0x3a800000, v151
	v_fmamk_f32 v84, v84, 0x3a800000, v152
	v_fmamk_f32 v85, v85, 0x3a800000, v153
	v_fmamk_f32 v18, v18, 0x3a800000, v134
	v_fmamk_f32 v19, v19, 0x3a800000, v135
	v_fmamk_f32 v20, v20, 0x3a800000, v136
	v_fmamk_f32 v21, v21, 0x3a800000, v137
	global_store_dword v208, v228, s[96:97]
	global_store_dword v209, v229, s[96:97]
	v_cvt_pk_fp8_f32 v230, v82, v83
	v_cvt_pk_fp8_f32 v231, v84, v85
	v_cvt_pk_fp8_f32 v230, v18, v19 op_sel:[0,0,1]
	v_cvt_pk_fp8_f32 v231, v20, v21 op_sel:[0,0,1]
	v_fmamk_f32 v94, v94, 0x3a800000, v150
	v_fmamk_f32 v95, v95, 0x3a800000, v151
	v_fmamk_f32 v96, v96, 0x3a800000, v152
	v_fmamk_f32 v97, v97, 0x3a800000, v153
	v_fmamk_f32 v30, v30, 0x3a800000, v134
	v_fmamk_f32 v31, v31, 0x3a800000, v135
	v_fmamk_f32 v32, v32, 0x3a800000, v136
	v_fmamk_f32 v33, v33, 0x3a800000, v137
	global_store_dword v208, v230, s[96:97] offset:64
	global_store_dword v209, v231, s[96:97] offset:64
	v_cvt_pk_fp8_f32 v232, v94, v95
	v_cvt_pk_fp8_f32 v233, v96, v97
	v_cvt_pk_fp8_f32 v232, v30, v31 op_sel:[0,0,1]
	v_cvt_pk_fp8_f32 v233, v32, v33 op_sel:[0,0,1]
	v_fmamk_f32 v90, v90, 0x3a800000, v150
	v_fmamk_f32 v91, v91, 0x3a800000, v151
	v_fmamk_f32 v92, v92, 0x3a800000, v152
	v_fmamk_f32 v93, v93, 0x3a800000, v153
	v_fmamk_f32 v22, v22, 0x3a800000, v134
	v_fmamk_f32 v23, v23, 0x3a800000, v135
	v_fmamk_f32 v24, v24, 0x3a800000, v136
	v_fmamk_f32 v25, v25, 0x3a800000, v137
	global_store_dword v208, v232, s[96:97] offset:512
	global_store_dword v209, v233, s[96:97] offset:512
	v_cvt_pk_fp8_f32 v234, v90, v91
	v_cvt_pk_fp8_f32 v235, v92, v93
	v_cvt_pk_fp8_f32 v234, v22, v23 op_sel:[0,0,1]
	v_cvt_pk_fp8_f32 v235, v24, v25 op_sel:[0,0,1]
	v_fmamk_f32 v66, v66, 0x3a800000, v146
	v_fmamk_f32 v67, v67, 0x3a800000, v147
	v_fmamk_f32 v68, v68, 0x3a800000, v148
	v_fmamk_f32 v69, v69, 0x3a800000, v149
	v_fmamk_f32 v10, v10, 0x3a800000, v130
	v_fmamk_f32 v11, v11, 0x3a800000, v131
	v_fmamk_f32 v12, v12, 0x3a800000, v132
	v_fmamk_f32 v13, v13, 0x3a800000, v133
	global_store_dword v208, v234, s[96:97] offset:576
	global_store_dword v209, v235, s[96:97] offset:576
	v_cvt_pk_fp8_f32 v236, v66, v67
	v_cvt_pk_fp8_f32 v237, v68, v69
	v_cvt_pk_fp8_f32 v236, v10, v11 op_sel:[0,0,1]
	v_cvt_pk_fp8_f32 v237, v12, v13 op_sel:[0,0,1]
	v_fmamk_f32 v50, v50, 0x3a800000, v146
	v_fmamk_f32 v51, v51, 0x3a800000, v147
	v_fmamk_f32 v52, v52, 0x3a800000, v148
	v_fmamk_f32 v53, v53, 0x3a800000, v149
	v_fmamk_f32 v2, v2, 0x3a800000, v130
	v_fmamk_f32 v3, v3, 0x3a800000, v131
	v_fmamk_f32 v4, v4, 0x3a800000, v132
	v_fmamk_f32 v5, v5, 0x3a800000, v133
	global_store_dword v210, v236, s[96:97]
	global_store_dword v211, v237, s[96:97]
	v_cvt_pk_fp8_f32 v238, v50, v51
	v_cvt_pk_fp8_f32 v239, v52, v53
	v_cvt_pk_fp8_f32 v238, v2, v3 op_sel:[0,0,1]
	v_cvt_pk_fp8_f32 v239, v4, v5 op_sel:[0,0,1]
	v_fmamk_f32 v78, v78, 0x3a800000, v146
	v_fmamk_f32 v79, v79, 0x3a800000, v147
	v_fmamk_f32 v80, v80, 0x3a800000, v148
	v_fmamk_f32 v81, v81, 0x3a800000, v149
	v_fmamk_f32 v14, v14, 0x3a800000, v130
	v_fmamk_f32 v15, v15, 0x3a800000, v131
	v_fmamk_f32 v16, v16, 0x3a800000, v132
	v_fmamk_f32 v17, v17, 0x3a800000, v133
	global_store_dword v210, v238, s[96:97] offset:64
	global_store_dword v211, v239, s[96:97] offset:64
	v_cvt_pk_fp8_f32 v240, v78, v79
	v_cvt_pk_fp8_f32 v241, v80, v81
	v_cvt_pk_fp8_f32 v240, v14, v15 op_sel:[0,0,1]
	v_cvt_pk_fp8_f32 v241, v16, v17 op_sel:[0,0,1]
	v_fmamk_f32 v74, v74, 0x3a800000, v146
	v_fmamk_f32 v75, v75, 0x3a800000, v147
	v_fmamk_f32 v76, v76, 0x3a800000, v148
	v_fmamk_f32 v77, v77, 0x3a800000, v149
	v_fmamk_f32 v6, v6, 0x3a800000, v130
	v_fmamk_f32 v7, v7, 0x3a800000, v131
	v_fmamk_f32 v8, v8, 0x3a800000, v132
	v_fmamk_f32 v9, v9, 0x3a800000, v133
	global_store_dword v210, v240, s[96:97] offset:512
	global_store_dword v211, v241, s[96:97] offset:512
	v_cvt_pk_fp8_f32 v242, v74, v75
	v_cvt_pk_fp8_f32 v243, v76, v77
	v_cvt_pk_fp8_f32 v242, v6, v7 op_sel:[0,0,1]
	v_cvt_pk_fp8_f32 v243, v8, v9 op_sel:[0,0,1]
	s_nop 1
	global_store_dword v210, v242, s[96:97] offset:576
	global_store_dword v211, v243, s[96:97] offset:576
	s_mov_b64 s[56:57], 0
	s_andn2_b64 vcc, exec, s[52:53]
	s_mov_b32 s50, s54
	s_cbranch_vccz .LBB2_26
	s_branch .LBB2_8
.Lg2_v_epi:
	s_lshr_b32 s95, s50, 12
	s_lshl_b32 s95, s95, 8
	s_and_b32 s96, s94, 0x3ff
	s_lshr_b32 s96, s96, 2
	s_add_u32 s95, s95, s96
	s_add_u32 s95, s95, 0x800
	s_lshl_b32 s95, s95, 14
	s_add_u32 s96, s18, s95
	s_addc_u32 s97, s19, 0
	v_lshrrev_b32_e32 v200, 8, v0
	v_bfe_u32 v201, v0, 4, 2
	v_lshl_add_u32 v200, v200, 4, v201
	v_lshlrev_b32_e32 v200, 14, v200
	v_and_b32_e32 v202, 15, v0
	v_lshrrev_b32_e32 v201, 1, v0
	v_and_b32_e32 v201, 0x60, v201
	v_or3_b32 v202, v201, v202, s50
	v_and_b32_e32 v202, 0xfff, v202
	v_lshl_add_u32 v203, v202, 2, v200
	v_mov_b32_e32 v204, v203
	v_add_u32_e32 v205, 0x10000, v203
	v_add_u32_e32 v206, 0x20000, v203
	v_add_u32_e32 v207, 0x30000, v203
	v_add_u32_e32 v208, 0x80000, v203
	v_add_u32_e32 v209, 0x90000, v203
	v_add_u32_e32 v210, 0xa0000, v203
	v_add_u32_e32 v211, 0xb0000, v203
	v_fmamk_f32 v126, v126, 0x3a800000, v158
	v_fmamk_f32 v127, v127, 0x3a800000, v159
	v_fmamk_f32 v128, v128, 0x3a800000, v160
	v_fmamk_f32 v129, v129, 0x3a800000, v161
	v_fmamk_f32 v122, v122, 0x3a800000, v158
	v_fmamk_f32 v123, v123, 0x3a800000, v159
	v_fmamk_f32 v124, v124, 0x3a800000, v160
	v_fmamk_f32 v125, v125, 0x3a800000, v161
	v_cvt_pk_fp8_f32 v212, v126, v127
	v_cvt_pk_fp8_f32 v213, v122, v123
	v_cvt_pk_fp8_f32 v212, v128, v129 op_sel:[0,0,1]
	v_cvt_pk_fp8_f32 v213, v124, v125 op_sel:[0,0,1]
	v_fmamk_f32 v118, v118, 0x3a800000, v158
	v_fmamk_f32 v119, v119, 0x3a800000, v159
	v_fmamk_f32 v120, v120, 0x3a800000, v160
	v_fmamk_f32 v121, v121, 0x3a800000, v161
	v_fmamk_f32 v114, v114, 0x3a800000, v158
	v_fmamk_f32 v115, v115, 0x3a800000, v159
	v_fmamk_f32 v116, v116, 0x3a800000, v160
	v_fmamk_f32 v117, v117, 0x3a800000, v161
	global_store_dword v204, v212, s[96:97]
	global_store_dword v204, v213, s[96:97] offset:64
	v_cvt_pk_fp8_f32 v214, v118, v119
	v_cvt_pk_fp8_f32 v215, v114, v115
	v_cvt_pk_fp8_f32 v214, v120, v121 op_sel:[0,0,1]
	v_cvt_pk_fp8_f32 v215, v116, v117 op_sel:[0,0,1]
	v_fmamk_f32 v110, v110, 0x3a800000, v154
	v_fmamk_f32 v111, v111, 0x3a800000, v155
	v_fmamk_f32 v112, v112, 0x3a800000, v156
	v_fmamk_f32 v113, v113, 0x3a800000, v157
	v_fmamk_f32 v98, v98, 0x3a800000, v154
	v_fmamk_f32 v99, v99, 0x3a800000, v155
	v_fmamk_f32 v100, v100, 0x3a800000, v156
	v_fmamk_f32 v101, v101, 0x3a800000, v157
	global_store_dword v204, v214, s[96:97] offset:512
	global_store_dword v204, v215, s[96:97] offset:576
	v_cvt_pk_fp8_f32 v216, v110, v111
	v_cvt_pk_fp8_f32 v217, v98, v99
	v_cvt_pk_fp8_f32 v216, v112, v113 op_sel:[0,0,1]
	v_cvt_pk_fp8_f32 v217, v100, v101 op_sel:[0,0,1]
	v_fmamk_f32 v106, v106, 0x3a800000, v154
	v_fmamk_f32 v107, v107, 0x3a800000, v155
	v_fmamk_f32 v108, v108, 0x3a800000, v156
	v_fmamk_f32 v109, v109, 0x3a800000, v157
	v_fmamk_f32 v102, v102, 0x3a800000, v154
	v_fmamk_f32 v103, v103, 0x3a800000, v155
	v_fmamk_f32 v104, v104, 0x3a800000, v156
	v_fmamk_f32 v105, v105, 0x3a800000, v157
	global_store_dword v205, v216, s[96:97]
	global_store_dword v205, v217, s[96:97] offset:64
	v_cvt_pk_fp8_f32 v218, v106, v107
	v_cvt_pk_fp8_f32 v219, v102, v103
	v_cvt_pk_fp8_f32 v218, v108, v109 op_sel:[0,0,1]
	v_cvt_pk_fp8_f32 v219, v104, v105 op_sel:[0,0,1]
	v_fmamk_f32 v86, v86, 0x3a800000, v150
	v_fmamk_f32 v87, v87, 0x3a800000, v151
	v_fmamk_f32 v88, v88, 0x3a800000, v152
	v_fmamk_f32 v89, v89, 0x3a800000, v153
	v_fmamk_f32 v82, v82, 0x3a800000, v150
	v_fmamk_f32 v83, v83, 0x3a800000, v151
	v_fmamk_f32 v84, v84, 0x3a800000, v152
	v_fmamk_f32 v85, v85, 0x3a800000, v153
	global_store_dword v205, v218, s[96:97] offset:512
	global_store_dword v205, v219, s[96:97] offset:576
	v_cvt_pk_fp8_f32 v220, v86, v87
	v_cvt_pk_fp8_f32 v221, v82, v83
	v_cvt_pk_fp8_f32 v220, v88, v89 op_sel:[0,0,1]
	v_cvt_pk_fp8_f32 v221, v84, v85 op_sel:[0,0,1]
	v_fmamk_f32 v94, v94, 0x3a800000, v150
	v_fmamk_f32 v95, v95, 0x3a800000, v151
	v_fmamk_f32 v96, v96, 0x3a800000, v152
	v_fmamk_f32 v97, v97, 0x3a800000, v153
	v_fmamk_f32 v90, v90, 0x3a800000, v150
	v_fmamk_f32 v91, v91, 0x3a800000, v151
	v_fmamk_f32 v92, v92, 0x3a800000, v152
	v_fmamk_f32 v93, v93, 0x3a800000, v153
	global_store_dword v206, v220, s[96:97]
	global_store_dword v206, v221, s[96:97] offset:64
	v_cvt_pk_fp8_f32 v222, v94, v95
	v_cvt_pk_fp8_f32 v223, v90, v91
	v_cvt_pk_fp8_f32 v222, v96, v97 op_sel:[0,0,1]
	v_cvt_pk_fp8_f32 v223, v92, v93 op_sel:[0,0,1]
	v_fmamk_f32 v66, v66, 0x3a800000, v146
	v_fmamk_f32 v67, v67, 0x3a800000, v147
	v_fmamk_f32 v68, v68, 0x3a800000, v148
	v_fmamk_f32 v69, v69, 0x3a800000, v149
	v_fmamk_f32 v50, v50, 0x3a800000, v146
	v_fmamk_f32 v51, v51, 0x3a800000, v147
	v_fmamk_f32 v52, v52, 0x3a800000, v148
	v_fmamk_f32 v53, v53, 0x3a800000, v149
	global_store_dword v206, v222, s[96:97] offset:512
	global_store_dword v206, v223, s[96:97] offset:576
	v_cvt_pk_fp8_f32 v224, v66, v67
	v_cvt_pk_fp8_f32 v225, v50, v51
	v_cvt_pk_fp8_f32 v224, v68, v69 op_sel:[0,0,1]
	v_cvt_pk_fp8_f32 v225, v52, v53 op_sel:[0,0,1]
	v_fmamk_f32 v78, v78, 0x3a800000, v146
	v_fmamk_f32 v79, v79, 0x3a800000, v147
	v_fmamk_f32 v80, v80, 0x3a800000, v148
	v_fmamk_f32 v81, v81, 0x3a800000, v149
	v_fmamk_f32 v74, v74, 0x3a800000, v146
	v_fmamk_f32 v75, v75, 0x3a800000, v147
	v_fmamk_f32 v76, v76, 0x3a800000, v148
	v_fmamk_f32 v77, v77, 0x3a800000, v149
	global_store_dword v207, v224, s[96:97]
	global_store_dword v207, v225, s[96:97] offset:64
	v_cvt_pk_fp8_f32 v226, v78, v79
	v_cvt_pk_fp8_f32 v227, v74, v75
	v_cvt_pk_fp8_f32 v226, v80, v81 op_sel:[0,0,1]
	v_cvt_pk_fp8_f32 v227, v76, v77 op_sel:[0,0,1]
	v_fmamk_f32 v62, v62, 0x3a800000, v142
	v_fmamk_f32 v63, v63, 0x3a800000, v143
	v_fmamk_f32 v64, v64, 0x3a800000, v144
	v_fmamk_f32 v65, v65, 0x3a800000, v145
	v_fmamk_f32 v54, v54, 0x3a800000, v142
	v_fmamk_f32 v55, v55, 0x3a800000, v143
	v_fmamk_f32 v56, v56, 0x3a800000, v144
	v_fmamk_f32 v57, v57, 0x3a800000, v145
	global_store_dword v207, v226, s[96:97] offset:512
	global_store_dword v207, v227, s[96:97] offset:576
	v_cvt_pk_fp8_f32 v228, v62, v63
	v_cvt_pk_fp8_f32 v229, v54, v55
	v_cvt_pk_fp8_f32 v228, v64, v65 op_sel:[0,0,1]
	v_cvt_pk_fp8_f32 v229, v56, v57 op_sel:[0,0,1]
	v_fmamk_f32 v70, v70, 0x3a800000, v142
	v_fmamk_f32 v71, v71, 0x3a800000, v143
	v_fmamk_f32 v72, v72, 0x3a800000, v144
	v_fmamk_f32 v73, v73, 0x3a800000, v145
	v_fmamk_f32 v58, v58, 0x3a800000, v142
	v_fmamk_f32 v59, v59, 0x3a800000, v143
	v_fmamk_f32 v60, v60, 0x3a800000, v144
	v_fmamk_f32 v61, v61, 0x3a800000, v145
	global_store_dword v208, v228, s[96:97]
	global_store_dword v208, v229, s[96:97] offset:64
	v_cvt_pk_fp8_f32 v230, v70, v71
	v_cvt_pk_fp8_f32 v231, v58, v59
	v_cvt_pk_fp8_f32 v230, v72, v73 op_sel:[0,0,1]
	v_cvt_pk_fp8_f32 v231, v60, v61 op_sel:[0,0,1]
	v_fmamk_f32 v42, v42, 0x3a800000, v138
	v_fmamk_f32 v43, v43, 0x3a800000, v139
	v_fmamk_f32 v44, v44, 0x3a800000, v140
	v_fmamk_f32 v45, v45, 0x3a800000, v141
	v_fmamk_f32 v34, v34, 0x3a800000, v138
	v_fmamk_f32 v35, v35, 0x3a800000, v139
	v_fmamk_f32 v36, v36, 0x3a800000, v140
	v_fmamk_f32 v37, v37, 0x3a800000, v141
	global_store_dword v208, v230, s[96:97] offset:512
	global_store_dword v208, v231, s[96:97] offset:576
	v_cvt_pk_fp8_f32 v232, v42, v43
	v_cvt_pk_fp8_f32 v233, v34, v35
	v_cvt_pk_fp8_f32 v232, v44, v45 op_sel:[0,0,1]
	v_cvt_pk_fp8_f32 v233, v36, v37 op_sel:[0,0,1]
	v_fmamk_f32 v46, v46, 0x3a800000, v138
	v_fmamk_f32 v47, v47, 0x3a800000, v139
	v_fmamk_f32 v48, v48, 0x3a800000, v140
	v_fmamk_f32 v49, v49, 0x3a800000, v141
	v_fmamk_f32 v38, v38, 0x3a800000, v138
	v_fmamk_f32 v39, v39, 0x3a800000, v139
	v_fmamk_f32 v40, v40, 0x3a800000, v140
	v_fmamk_f32 v41, v41, 0x3a800000, v141
	global_store_dword v209, v232, s[96:97]
	global_store_dword v209, v233, s[96:97] offset:64
	v_cvt_pk_fp8_f32 v234, v46, v47
	v_cvt_pk_fp8_f32 v235, v38, v39
	v_cvt_pk_fp8_f32 v234, v48, v49 op_sel:[0,0,1]
	v_cvt_pk_fp8_f32 v235, v40, v41 op_sel:[0,0,1]
	v_fmamk_f32 v26, v26, 0x3a800000, v134
	v_fmamk_f32 v27, v27, 0x3a800000, v135
	v_fmamk_f32 v28, v28, 0x3a800000, v136
	v_fmamk_f32 v29, v29, 0x3a800000, v137
	v_fmamk_f32 v18, v18, 0x3a800000, v134
	v_fmamk_f32 v19, v19, 0x3a800000, v135
	v_fmamk_f32 v20, v20, 0x3a800000, v136
	v_fmamk_f32 v21, v21, 0x3a800000, v137
	global_store_dword v209, v234, s[96:97] offset:512
	global_store_dword v209, v235, s[96:97] offset:576
	v_cvt_pk_fp8_f32 v236, v26, v27
	v_cvt_pk_fp8_f32 v237, v18, v19
	v_cvt_pk_fp8_f32 v236, v28, v29 op_sel:[0,0,1]
	v_cvt_pk_fp8_f32 v237, v20, v21 op_sel:[0,0,1]
	v_fmamk_f32 v30, v30, 0x3a800000, v134
	v_fmamk_f32 v31, v31, 0x3a800000, v135
	v_fmamk_f32 v32, v32, 0x3a800000, v136
	v_fmamk_f32 v33, v33, 0x3a800000, v137
	v_fmamk_f32 v22, v22, 0x3a800000, v134
	v_fmamk_f32 v23, v23, 0x3a800000, v135
	v_fmamk_f32 v24, v24, 0x3a800000, v136
	v_fmamk_f32 v25, v25, 0x3a800000, v137
	global_store_dword v210, v236, s[96:97]
	global_store_dword v210, v237, s[96:97] offset:64
	v_cvt_pk_fp8_f32 v238, v30, v31
	v_cvt_pk_fp8_f32 v239, v22, v23
	v_cvt_pk_fp8_f32 v238, v32, v33 op_sel:[0,0,1]
	v_cvt_pk_fp8_f32 v239, v24, v25 op_sel:[0,0,1]
	v_fmamk_f32 v10, v10, 0x3a800000, v130
	v_fmamk_f32 v11, v11, 0x3a800000, v131
	v_fmamk_f32 v12, v12, 0x3a800000, v132
	v_fmamk_f32 v13, v13, 0x3a800000, v133
	v_fmamk_f32 v2, v2, 0x3a800000, v130
	v_fmamk_f32 v3, v3, 0x3a800000, v131
	v_fmamk_f32 v4, v4, 0x3a800000, v132
	v_fmamk_f32 v5, v5, 0x3a800000, v133
	global_store_dword v210, v238, s[96:97] offset:512
	global_store_dword v210, v239, s[96:97] offset:576
	v_cvt_pk_fp8_f32 v240, v10, v11
	v_cvt_pk_fp8_f32 v241, v2, v3
	v_cvt_pk_fp8_f32 v240, v12, v13 op_sel:[0,0,1]
	v_cvt_pk_fp8_f32 v241, v4, v5 op_sel:[0,0,1]
	v_fmamk_f32 v14, v14, 0x3a800000, v130
	v_fmamk_f32 v15, v15, 0x3a800000, v131
	v_fmamk_f32 v16, v16, 0x3a800000, v132
	v_fmamk_f32 v17, v17, 0x3a800000, v133
	v_fmamk_f32 v6, v6, 0x3a800000, v130
	v_fmamk_f32 v7, v7, 0x3a800000, v131
	v_fmamk_f32 v8, v8, 0x3a800000, v132
	v_fmamk_f32 v9, v9, 0x3a800000, v133
	global_store_dword v211, v240, s[96:97]
	global_store_dword v211, v241, s[96:97] offset:64
	v_cvt_pk_fp8_f32 v242, v14, v15
	v_cvt_pk_fp8_f32 v243, v6, v7
	v_cvt_pk_fp8_f32 v242, v16, v17 op_sel:[0,0,1]
	v_cvt_pk_fp8_f32 v243, v8, v9 op_sel:[0,0,1]
	s_nop 1
	global_store_dword v211, v242, s[96:97] offset:512
	global_store_dword v211, v243, s[96:97] offset:576
	s_mov_b64 s[56:57], 0
	s_andn2_b64 vcc, exec, s[52:53]
	s_mov_b32 s50, s54
	s_cbranch_vccz .LBB2_26
	s_branch .LBB2_8
.LBB2_26:
	s_endpgm
	s_nop 0
	s_nop 0
	s_nop 0
	s_nop 0
	s_nop 0
	s_nop 0
	s_nop 0
	s_nop 0
	s_nop 0
	s_nop 0
	s_nop 0
	s_nop 0
	s_nop 0
	s_nop 0
	s_nop 0
	s_nop 0
	s_nop 0
	s_nop 0
	s_nop 0
	s_nop 0
	s_nop 0
	s_nop 0
	s_nop 0
	s_nop 0
	s_nop 0
	s_nop 0
	s_nop 0
	s_nop 0
	s_endpgm
